# speedup vs baseline: 1.0043x; 1.0043x over previous
.LBB13_10:
	s_or_b64 exec, exec, s[4:5]
	s_waitcnt lgkmcnt(0)
	v_lshl_or_b32 v12, v98, 2, s6
	v_add_u32_e32 v14, 0x4800, v12
	s_barrier
	v_add_u32_e32 v10, 0x4000, v12
	v_add_u32_e32 v13, 0x4400, v12
	ds_read2_b32 v[0:1], v14 offset0:128 offset1:160
	ds_read2_b32 v[2:3], v13 offset0:192 offset1:224
	ds_read2_b32 v[4:5], v10 offset1:32
	ds_read2_b32 v[6:7], v10 offset0:192 offset1:224
	s_add_u32 s0, s0, s2
	s_waitcnt lgkmcnt(3)
	v_max_f32_e32 v8, v1, v1
	s_waitcnt lgkmcnt(2)
	v_max_f32_e32 v9, v2, v2
	v_max_f32_e32 v8, v9, v8
	s_waitcnt lgkmcnt(0)
	v_max3_f32 v15, v4, v7, v8
	v_sub_f32_e32 v4, v4, v15
	v_exp_f32_e32 v50, v4
	ds_read2_b32 v[8:9], v10 offset0:64 offset1:96
	ds_read2_b32 v[10:11], v10 offset0:128 offset1:160
	v_sub_f32_e32 v7, v7, v15
	v_fma_f32 v51, v5, v50, 0
	ds_read2_b32 v[4:5], v13 offset1:32
	v_exp_f32_e32 v54, v7
	s_waitcnt lgkmcnt(2)
	v_fma_f32 v52, v8, v50, 0
	v_sub_f32_e32 v2, v2, v15
	v_fma_f32 v53, v50, v9, 0
	s_waitcnt lgkmcnt(1)
	v_fma_f32 v10, v50, v10, 0
	ds_read2_b32 v[8:9], v13 offset0:64 offset1:96
	v_fma_f32 v11, v50, v11, 0
	v_fma_f32 v50, v50, v6, 0
	s_waitcnt lgkmcnt(1)
	v_fmac_f32_e32 v51, v4, v54
	v_fmac_f32_e32 v52, v5, v54
	ds_read2_b32 v[4:5], v13 offset0:128 offset1:160
	v_exp_f32_e32 v13, v2
	ds_read2_b32 v[6:7], v14 offset1:32
	v_sub_f32_e32 v1, v1, v15
	s_waitcnt lgkmcnt(2)
	v_fmac_f32_e32 v53, v54, v8
	v_fmac_f32_e32 v51, v3, v13
	ds_read2_b32 v[2:3], v14 offset0:192 offset1:224
	s_waitcnt lgkmcnt(1)
	v_fmac_f32_e32 v52, v6, v13
	v_exp_f32_e32 v6, v1
	v_fmac_f32_e32 v10, v54, v9
	ds_read2_b32 v[8:9], v14 offset0:64 offset1:96
	v_fmac_f32_e32 v50, v54, v5
	v_add_u32_e32 v1, 0x4c00, v12
	s_waitcnt lgkmcnt(1)
	v_fmac_f32_e32 v51, v2, v6
	s_mov_b32 s4, 0x3f317218
	s_addc_u32 s1, s1, s3
	v_fmac_f32_e32 v11, v54, v4
	ds_read2_b32 v[4:5], v1 offset1:32
	v_fmac_f32_e32 v50, v13, v0
	ds_read2_b32 v[0:1], v1 offset0:64 offset1:96
	v_div_scale_f32 v2, s[2:3], v51, v51, s4
	v_fmac_f32_e32 v52, v3, v6
	v_rcp_f32_e32 v3, v2
	s_waitcnt lgkmcnt(2)
	v_fmac_f32_e32 v11, v13, v9
	s_waitcnt lgkmcnt(0)
	v_fmac_f32_e32 v11, v6, v0
	v_fmac_f32_e32 v53, v13, v7
	v_fma_f32 v0, -v2, v3, 1.0
	v_fmac_f32_e32 v3, v0, v3
	v_div_scale_f32 v0, vcc, s4, v51, s4
	v_fmac_f32_e32 v50, v6, v1
	v_mul_f32_e32 v1, v0, v3
	v_fmac_f32_e32 v53, v6, v4
	v_fma_f32 v4, -v2, v1, v0
	v_fmac_f32_e32 v1, v4, v3
	v_fma_f32 v0, -v2, v1, v0
	v_fmac_f32_e32 v10, v13, v8
	v_div_fmas_f32 v0, v0, v3, v1
	v_fmac_f32_e32 v10, v6, v5
	v_div_fixup_f32 v0, v0, v51, s4
	v_mul_f32_e32 v2, v52, v0
	v_mul_f32_e32 v4, v53, v0
	v_mul_f32_e32 v3, v10, v0
	v_mul_f32_e32 v1, v11, v0
	v_mul_f32_e32 v0, v50, v0
	v_lshrrev_b32_e32 v98, 6, v97
	v_lshlrev_b32_e32 v98, 8, v98
	v_and_b32_e32 v99, 4, v97
	v_lshl_or_b32 v98, v99, 8, v98
	v_and_b32_e32 v99, 0x7c, v96
	v_or_b32_e32 v98, v98, v99
	v_add_u32_e32 v98, 0x10800, v98
	ds_read_b32 v99, v98
	ds_read_b32 v100, v98 offset:2048
	ds_read_b32 v101, v98 offset:4096
	ds_read_b32 v102, v98 offset:128
	ds_read_b32 v103, v98 offset:2176
	ds_read_b32 v104, v98 offset:4224
	s_mov_b32 s42, 0
	s_mov_b32 s43, -1
	v_cndmask_b32_e64 v105, v2, v4, s[42:43]
	v_cndmask_b32_e64 v106, v3, v1, s[42:43]
	v_mov_b32_e32 v107, 1.0
	v_cndmask_b32_e64 v107, v0, v107, s[42:43]
	s_waitcnt lgkmcnt(0)
	v_mfma_f32_32x32x2_f32 v[44:59], v99, v105, 0
	v_mfma_f32_32x32x2_f32 v[112:127], v102, v105, 0
	v_mfma_f32_32x32x2_f32 v[44:59], v100, v106, v[44:59]
	v_mfma_f32_32x32x2_f32 v[112:127], v103, v106, v[112:127]
	v_mfma_f32_32x32x2_f32 v[44:59], v101, v107, v[44:59]
	v_mfma_f32_32x32x2_f32 v[112:127], v104, v107, v[112:127]
	s_nop 15
	s_nop 3
	v_mov_b32_e32 v14, v96
	v_add_f32_e32 v6, v110, v44
	global_store_dword v14, v6, s[0:1] nt
	s_add_u32 s40, s0, 0x4000
	s_addc_u32 s41, s1, 0
	v_add_f32_e32 v6, v72, v45
	global_store_dword v14, v6, s[40:41] nt
	s_add_u32 s40, s0, 0x8000
	s_addc_u32 s41, s1, 0
	v_add_f32_e32 v6, v73, v46
	global_store_dword v14, v6, s[40:41] nt
	s_add_u32 s40, s0, 0xc000
	s_addc_u32 s41, s1, 0
	v_add_f32_e32 v6, v74, v47
	global_store_dword v14, v6, s[40:41] nt
	v_mov_b32_e32 v14, v96
	s_add_u32 s40, s0, 0x20000
	s_addc_u32 s41, s1, 0
	v_add_f32_e32 v6, v76, v48
	global_store_dword v14, v6, s[40:41] nt
	s_add_u32 s40, s0, 0x24000
	s_addc_u32 s41, s1, 0
	v_add_f32_e32 v6, v75, v49
	global_store_dword v14, v6, s[40:41] nt
	s_add_u32 s40, s0, 0x28000
	s_addc_u32 s41, s1, 0
	v_add_f32_e32 v6, v85, v50
	global_store_dword v14, v6, s[40:41] nt
	s_add_u32 s40, s0, 0x2c000
	s_addc_u32 s41, s1, 0
	v_add_f32_e32 v6, v83, v51
	global_store_dword v14, v6, s[40:41] nt
	v_mov_b32_e32 v14, v96
	s_add_u32 s40, s0, 0x40000
	s_addc_u32 s41, s1, 0
	v_add_f32_e32 v6, v68, v52
	global_store_dword v14, v6, s[40:41] nt
	s_add_u32 s40, s0, 0x44000
	s_addc_u32 s41, s1, 0
	v_add_f32_e32 v6, v60, v53
	global_store_dword v14, v6, s[40:41] nt
	s_add_u32 s40, s0, 0x48000
	s_addc_u32 s41, s1, 0
	v_add_f32_e32 v6, v64, v54
	global_store_dword v14, v6, s[40:41] nt
	s_add_u32 s40, s0, 0x4c000
	s_addc_u32 s41, s1, 0
	v_add_f32_e32 v6, v61, v55
	global_store_dword v14, v6, s[40:41] nt
	v_mov_b32_e32 v14, v96
	s_add_u32 s40, s0, 0x60000
	s_addc_u32 s41, s1, 0
	v_add_f32_e32 v6, v71, v56
	global_store_dword v14, v6, s[40:41] nt
	s_add_u32 s40, s0, 0x64000
	s_addc_u32 s41, s1, 0
	v_add_f32_e32 v6, v70, v57
	global_store_dword v14, v6, s[40:41] nt
	s_add_u32 s40, s0, 0x68000
	s_addc_u32 s41, s1, 0
	v_add_f32_e32 v6, v88, v58
	global_store_dword v14, v6, s[40:41] nt
	s_add_u32 s40, s0, 0x6c000
	s_addc_u32 s41, s1, 0
	v_add_f32_e32 v6, v86, v59
	global_store_dword v14, v6, s[40:41] nt
	v_mov_b32_e32 v14, v96
	s_add_u32 s40, s0, 0x80000
	s_addc_u32 s41, s1, 0
	v_add_f32_e32 v6, v25, v112
	global_store_dword v14, v6, s[40:41] nt
	s_add_u32 s40, s0, 0x84000
	s_addc_u32 s41, s1, 0
	v_add_f32_e32 v6, v24, v113
	global_store_dword v14, v6, s[40:41] nt
	s_add_u32 s40, s0, 0x88000
	s_addc_u32 s41, s1, 0
	v_add_f32_e32 v6, v28, v114
	global_store_dword v14, v6, s[40:41] nt
	s_add_u32 s40, s0, 0x8c000
	s_addc_u32 s41, s1, 0
	v_add_f32_e32 v6, v26, v115
	global_store_dword v14, v6, s[40:41] nt
	v_mov_b32_e32 v14, v96
	s_add_u32 s40, s0, 0xa0000
	s_addc_u32 s41, s1, 0
	v_add_f32_e32 v6, v20, v116
	global_store_dword v14, v6, s[40:41] nt
	s_add_u32 s40, s0, 0xa4000
	s_addc_u32 s41, s1, 0
	v_add_f32_e32 v6, v21, v117
	global_store_dword v14, v6, s[40:41] nt
	s_add_u32 s40, s0, 0xa8000
	s_addc_u32 s41, s1, 0
	v_add_f32_e32 v6, v22, v118
	global_store_dword v14, v6, s[40:41] nt
	s_add_u32 s40, s0, 0xac000
	s_addc_u32 s41, s1, 0
	v_add_f32_e32 v6, v23, v119
	global_store_dword v14, v6, s[40:41] nt
	v_mov_b32_e32 v14, v96
	s_add_u32 s40, s0, 0xc0000
	s_addc_u32 s41, s1, 0
	v_add_f32_e32 v6, v42, v120
	global_store_dword v14, v6, s[40:41] nt
	s_add_u32 s40, s0, 0xc4000
	s_addc_u32 s41, s1, 0
	v_add_f32_e32 v6, v40, v121
	global_store_dword v14, v6, s[40:41] nt
	s_add_u32 s40, s0, 0xc8000
	s_addc_u32 s41, s1, 0
	v_add_f32_e32 v6, v39, v122
	global_store_dword v14, v6, s[40:41] nt
	s_add_u32 s40, s0, 0xcc000
	s_addc_u32 s41, s1, 0
	v_add_f32_e32 v6, v43, v123
	global_store_dword v14, v6, s[40:41] nt
	s_add_u32 s40, s0, 0xe0000
	s_addc_u32 s41, s1, 0
	v_add_f32_e32 v5, v16, v124
	global_store_dword v96, v5, s[40:41] nt
	s_add_u32 s40, s0, 0xe4000
	s_addc_u32 s41, s1, 0
	v_add_f32_e32 v5, v17, v125
	global_store_dword v96, v5, s[40:41] nt
	v_add_f32_e32 v5, v18, v126
	v_add_f32_e32 v0, v19, v127
	v_add_u32_e32 v6, 0xe8000, v96
	v_add_u32_e32 v1, 0xec000, v96
	global_store_dword v6, v5, s[0:1] nt
	global_store_dword v1, v0, s[0:1] nt
	s_endpgm

	.amdhsa_kernel _Z12final_kernelPKtS0_PKfS2_S2_S2_S2_S2_S2_S2_S2_S2_S2_S2_PfPKhS5_
		.amdhsa_group_segment_fixed_size 74240
		.amdhsa_private_segment_fixed_size 0
		.amdhsa_kernarg_size 136
		.amdhsa_user_sgpr_count 2
		.amdhsa_user_sgpr_dispatch_ptr 0
		.amdhsa_user_sgpr_queue_ptr 0
		.amdhsa_user_sgpr_kernarg_segment_ptr 1
		.amdhsa_user_sgpr_dispatch_id 0
		.amdhsa_user_sgpr_kernarg_preload_length 0
		.amdhsa_user_sgpr_kernarg_preload_offset 0
		.amdhsa_user_sgpr_private_segment_size 0
		.amdhsa_uses_dynamic_stack 0
		.amdhsa_enable_private_segment 0
		.amdhsa_system_sgpr_workgroup_id_x 1
		.amdhsa_system_sgpr_workgroup_id_y 0
		.amdhsa_system_sgpr_workgroup_id_z 0
		.amdhsa_system_sgpr_workgroup_info 0
		.amdhsa_system_vgpr_workitem_id 0
		.amdhsa_next_free_vgpr 128
		.amdhsa_next_free_sgpr 96
		.amdhsa_accum_offset 128
		.amdhsa_reserve_vcc 1
		.amdhsa_float_round_mode_32 0
		.amdhsa_float_round_mode_16_64 0
		.amdhsa_float_denorm_mode_32 3
		.amdhsa_float_denorm_mode_16_64 3
		.amdhsa_dx10_clamp 1
		.amdhsa_ieee_mode 1
		.amdhsa_fp16_overflow 0
		.amdhsa_tg_split 0
		.amdhsa_exception_fp_ieee_invalid_op 0
		.amdhsa_exception_fp_denorm_src 0
		.amdhsa_exception_fp_ieee_div_zero 0
		.amdhsa_exception_fp_ieee_overflow 0
		.amdhsa_exception_fp_ieee_underflow 0
		.amdhsa_exception_fp_ieee_inexact 0
		.amdhsa_exception_int_div_zero 0
	.end_amdhsa_kernel

amdhsa.kernels:
  - .agpr_count:     0
    .args:
      - .actual_access:  read_only
        .address_space:  global
        .offset:         0
        .size:           8
        .value_kind:     global_buffer
      - .actual_access:  write_only
        .address_space:  global
        .offset:         8
        .size:           8
        .value_kind:     global_buffer
      - .actual_access:  write_only
        .address_space:  global
        .offset:         16
        .size:           8
        .value_kind:     global_buffer
      - .actual_access:  read_only
        .address_space:  global
        .offset:         24
        .size:           8
        .value_kind:     global_buffer
      - .actual_access:  read_only
        .address_space:  global
        .offset:         32
        .size:           8
        .value_kind:     global_buffer
      - .actual_access:  read_only
        .address_space:  global
        .offset:         40
        .size:           8
        .value_kind:     global_buffer
      - .actual_access:  read_only
        .address_space:  global
        .offset:         48
        .size:           8
        .value_kind:     global_buffer
      - .actual_access:  read_only
        .address_space:  global
        .offset:         56
        .size:           8
        .value_kind:     global_buffer
      - .actual_access:  read_only
        .address_space:  global
        .offset:         64
        .size:           8
        .value_kind:     global_buffer
      - .actual_access:  read_only
        .address_space:  global
        .offset:         72
        .size:           8
        .value_kind:     global_buffer
      - .actual_access:  read_only
        .address_space:  global
        .offset:         80
        .size:           8
        .value_kind:     global_buffer
      - .actual_access:  write_only
        .address_space:  global
        .offset:         88
        .size:           8
        .value_kind:     global_buffer
      - .actual_access:  write_only
        .address_space:  global
        .offset:         96
        .size:           8
        .value_kind:     global_buffer
      - .actual_access:  write_only
        .address_space:  global
        .offset:         104
        .size:           8
        .value_kind:     global_buffer
      - .actual_access:  write_only
        .address_space:  global
        .offset:         112
        .size:           8
        .value_kind:     global_buffer
      - .actual_access:  write_only
        .address_space:  global
        .offset:         120
        .size:           8
        .value_kind:     global_buffer
      - .actual_access:  write_only
        .address_space:  global
        .offset:         128
        .size:           8
        .value_kind:     global_buffer
      - .actual_access:  read_only
        .address_space:  global
        .offset:         136
        .size:           8
        .value_kind:     global_buffer
      - .actual_access:  read_only
        .address_space:  global
        .offset:         144
        .size:           8
        .value_kind:     global_buffer
    .group_segment_fixed_size: 0
    .kernarg_segment_align: 8
    .kernarg_segment_size: 152
    .language:       OpenCL C
    .language_version:
      - 2
      - 0
    .max_flat_workgroup_size: 256
    .name:           _Z11prep_kernelPKfPtPfS0_S0_S0_S0_S0_S0_S0_S0_S1_S1_S2_S2_S2_S1_S0_S2_
    .private_segment_fixed_size: 0
    .sgpr_count:     45
    .sgpr_spill_count: 0
    .symbol:         _Z11prep_kernelPKfPtPfS0_S0_S0_S0_S0_S0_S0_S0_S1_S1_S2_S2_S2_S1_S0_S2_.kd
    .uniform_work_group_size: 1
    .uses_dynamic_stack: false
    .vgpr_count:     53
    .vgpr_spill_count: 0
    .wavefront_size: 64
  - .agpr_count:     0
    .args:
      - .actual_access:  read_only
        .address_space:  global
        .offset:         0
        .size:           8
        .value_kind:     global_buffer
      - .actual_access:  write_only
        .address_space:  global
        .offset:         8
        .size:           8
        .value_kind:     global_buffer
      - .actual_access:  write_only
        .address_space:  global
        .offset:         16
        .size:           8
        .value_kind:     global_buffer
      - .offset:         24
        .size:           4
        .value_kind:     hidden_block_count_x
      - .offset:         28
        .size:           4
        .value_kind:     hidden_block_count_y
      - .offset:         32
        .size:           4
        .value_kind:     hidden_block_count_z
      - .offset:         36
        .size:           2
        .value_kind:     hidden_group_size_x
      - .offset:         38
        .size:           2
        .value_kind:     hidden_group_size_y
      - .offset:         40
        .size:           2
        .value_kind:     hidden_group_size_z
      - .offset:         42
        .size:           2
        .value_kind:     hidden_remainder_x
      - .offset:         44
        .size:           2
        .value_kind:     hidden_remainder_y
      - .offset:         46
        .size:           2
        .value_kind:     hidden_remainder_z
      - .offset:         64
        .size:           8
        .value_kind:     hidden_global_offset_x
      - .offset:         72
        .size:           8
        .value_kind:     hidden_global_offset_y
      - .offset:         80
        .size:           8
        .value_kind:     hidden_global_offset_z
      - .offset:         88
        .size:           2
        .value_kind:     hidden_grid_dims
    .group_segment_fixed_size: 0
    .kernarg_segment_align: 8
    .kernarg_segment_size: 280
    .language:       OpenCL C
    .language_version:
      - 2
      - 0
    .max_flat_workgroup_size: 256
    .name:           _Z12prep2_kernelPKfPtPf
    .private_segment_fixed_size: 0
    .sgpr_count:     26
    .sgpr_spill_count: 0
    .symbol:         _Z12prep2_kernelPKfPtPf.kd
    .uniform_work_group_size: 1
    .uses_dynamic_stack: false
    .vgpr_count:     56
    .vgpr_spill_count: 0
    .wavefront_size: 64
  - .agpr_count:     0
    .args:
      - .actual_access:  read_only
        .address_space:  global
        .offset:         0
        .size:           8
        .value_kind:     global_buffer
      - .actual_access:  read_only
        .address_space:  global
        .offset:         8
        .size:           8
        .value_kind:     global_buffer
      - .actual_access:  read_only
        .address_space:  global
        .offset:         16
        .size:           8
        .value_kind:     global_buffer
      - .actual_access:  write_only
        .address_space:  global
        .offset:         24
        .size:           8
        .value_kind:     global_buffer
      - .actual_access:  write_only
        .address_space:  global
        .offset:         32
        .size:           8
        .value_kind:     global_buffer
      - .actual_access:  write_only
        .address_space:  global
        .offset:         40
        .size:           8
        .value_kind:     global_buffer
    .group_segment_fixed_size: 0
    .kernarg_segment_align: 8
    .kernarg_segment_size: 48
    .language:       OpenCL C
    .language_version:
      - 2
      - 0
    .max_flat_workgroup_size: 256
    .name:           _Z9qkv_naivePKtS0_PKfPtS3_S3_
    .private_segment_fixed_size: 0
    .sgpr_count:     22
    .sgpr_spill_count: 0
    .symbol:         _Z9qkv_naivePKtS0_PKfPtS3_S3_.kd
    .uniform_work_group_size: 1
    .uses_dynamic_stack: false
    .vgpr_count:     25
    .vgpr_spill_count: 0
    .wavefront_size: 64
  - .agpr_count:     64
    .args:
      - .actual_access:  read_only
        .address_space:  global
        .offset:         0
        .size:           8
        .value_kind:     global_buffer
      - .actual_access:  read_only
        .address_space:  global
        .offset:         8
        .size:           8
        .value_kind:     global_buffer
      - .actual_access:  read_only
        .address_space:  global
        .offset:         16
        .size:           8
        .value_kind:     global_buffer
      - .actual_access:  write_only
        .address_space:  global
        .offset:         24
        .size:           8
        .value_kind:     global_buffer
      - .actual_access:  write_only
        .address_space:  global
        .offset:         32
        .size:           8
        .value_kind:     global_buffer
      - .actual_access:  write_only
        .address_space:  global
        .offset:         40
        .size:           8
        .value_kind:     global_buffer
    .group_segment_fixed_size: 36864
    .kernarg_segment_align: 8
    .kernarg_segment_size: 48
    .language:       OpenCL C
    .language_version:
      - 2
      - 0
    .max_flat_workgroup_size: 256
    .name:           _Z8qkv_mfmaPKtS0_PKfPtS3_S3_
    .private_segment_fixed_size: 0
    .sgpr_count:     24
    .sgpr_spill_count: 0
    .symbol:         _Z8qkv_mfmaPKtS0_PKfPtS3_S3_.kd
    .uniform_work_group_size: 1
    .uses_dynamic_stack: false
    .vgpr_count:     164
    .vgpr_spill_count: 0
    .wavefront_size: 64
  - .agpr_count:     0
    .args:
      - .actual_access:  read_only
        .address_space:  global
        .offset:         0
        .size:           8
        .value_kind:     global_buffer
      - .address_space:  global
        .offset:         8
        .size:           8
        .value_kind:     global_buffer
      - .actual_access:  read_only
        .address_space:  global
        .offset:         16
        .size:           8
        .value_kind:     global_buffer
      - .actual_access:  write_only
        .address_space:  global
        .offset:         24
        .size:           8
        .value_kind:     global_buffer
      - .actual_access:  write_only
        .address_space:  global
        .offset:         32
        .size:           8
        .value_kind:     global_buffer
      - .actual_access:  write_only
        .address_space:  global
        .offset:         40
        .size:           8
        .value_kind:     global_buffer
    .group_segment_fixed_size: 66048
    .kernarg_segment_align: 8
    .kernarg_segment_size: 48
    .language:       OpenCL C
    .language_version:
      - 2
      - 0
    .max_flat_workgroup_size: 256
    .name:           _Z10qkv_streamPKtS0_PKfPtS3_S3_
    .private_segment_fixed_size: 0
    .sgpr_count:     22
    .sgpr_spill_count: 0
    .symbol:         _Z10qkv_streamPKtS0_PKfPtS3_S3_.kd
    .uniform_work_group_size: 1
    .uses_dynamic_stack: false
    .vgpr_count:     230
    .vgpr_spill_count: 0
    .wavefront_size: 64
  - .agpr_count:     0
    .args:
      - .actual_access:  read_only
        .address_space:  global
        .offset:         0
        .size:           8
        .value_kind:     global_buffer
      - .actual_access:  read_only
        .address_space:  global
        .offset:         8
        .size:           8
        .value_kind:     global_buffer
      - .actual_access:  read_only
        .address_space:  global
        .offset:         16
        .size:           8
        .value_kind:     global_buffer
      - .actual_access:  write_only
        .address_space:  global
        .offset:         24
        .size:           8
        .value_kind:     global_buffer
    .group_segment_fixed_size: 0
    .kernarg_segment_align: 8
    .kernarg_segment_size: 32
    .language:       OpenCL C
    .language_version:
      - 2
      - 0
    .max_flat_workgroup_size: 256
    .name:           _Z10attn_naivePKtS0_S0_Pt
    .private_segment_fixed_size: 0
    .sgpr_count:     20
    .sgpr_spill_count: 0
    .symbol:         _Z10attn_naivePKtS0_S0_Pt.kd
    .uniform_work_group_size: 1
    .uses_dynamic_stack: false
    .vgpr_count:     108
    .vgpr_spill_count: 0
    .wavefront_size: 64
  - .agpr_count:     0
    .args:
      - .actual_access:  read_only
        .address_space:  global
        .offset:         0
        .size:           8
        .value_kind:     global_buffer
      - .address_space:  global
        .offset:         8
        .size:           8
        .value_kind:     global_buffer
      - .actual_access:  read_only
        .address_space:  global
        .offset:         16
        .size:           8
        .value_kind:     global_buffer
      - .actual_access:  read_only
        .address_space:  global
        .offset:         24
        .size:           8
        .value_kind:     global_buffer
      - .address_space:  global
        .offset:         32
        .size:           8
        .value_kind:     global_buffer
      - .actual_access:  write_only
        .address_space:  global
        .offset:         40
        .size:           8
        .value_kind:     global_buffer
      - .actual_access:  write_only
        .address_space:  global
        .offset:         48
        .size:           8
        .value_kind:     global_buffer
    .group_segment_fixed_size: 155648
    .kernarg_segment_align: 8
    .kernarg_segment_size: 56
    .language:       OpenCL C
    .language_version:
      - 2
      - 0
    .max_flat_workgroup_size: 512
    .name:           _Z9attn_mfmaPKtS0_PKfS2_PtS3_S3_
    .private_segment_fixed_size: 0
    .sgpr_count:     41
    .sgpr_spill_count: 0
    .symbol:         _Z9attn_mfmaPKtS0_PKfS2_PtS3_S3_.kd
    .uniform_work_group_size: 1
    .uses_dynamic_stack: false
    .vgpr_count:     215
    .vgpr_spill_count: 0
    .wavefront_size: 64
  - .agpr_count:     0
    .args:
      - .actual_access:  read_only
        .address_space:  global
        .offset:         0
        .size:           8
        .value_kind:     global_buffer
      - .actual_access:  read_only
        .address_space:  global
        .offset:         8
        .size:           8
        .value_kind:     global_buffer
      - .actual_access:  read_only
        .address_space:  global
        .offset:         16
        .size:           8
        .value_kind:     global_buffer
      - .actual_access:  read_only
        .address_space:  global
        .offset:         24
        .size:           8
        .value_kind:     global_buffer
      - .actual_access:  write_only
        .address_space:  global
        .offset:         32
        .size:           8
        .value_kind:     global_buffer
      - .actual_access:  write_only
        .address_space:  global
        .offset:         40
        .size:           8
        .value_kind:     global_buffer
    .group_segment_fixed_size: 0
    .kernarg_segment_align: 8
    .kernarg_segment_size: 48
    .language:       OpenCL C
    .language_version:
      - 2
      - 0
    .max_flat_workgroup_size: 256
    .name:           _Z11special_outPKtS0_PKfS2_PfS3_
    .private_segment_fixed_size: 0
    .sgpr_count:     28
    .sgpr_spill_count: 0
    .symbol:         _Z11special_outPKtS0_PKfS2_PfS3_.kd
    .uniform_work_group_size: 1
    .uses_dynamic_stack: false
    .vgpr_count:     15
    .vgpr_spill_count: 0
    .wavefront_size: 64
  - .agpr_count:     0
    .args:
      - .actual_access:  read_only
        .address_space:  global
        .offset:         0
        .size:           8
        .value_kind:     global_buffer
      - .actual_access:  read_only
        .address_space:  global
        .offset:         8
        .size:           8
        .value_kind:     global_buffer
      - .actual_access:  write_only
        .address_space:  global
        .offset:         16
        .size:           8
        .value_kind:     global_buffer
      - .actual_access:  write_only
        .address_space:  global
        .offset:         24
        .size:           8
        .value_kind:     global_buffer
    .group_segment_fixed_size: 0
    .kernarg_segment_align: 8
    .kernarg_segment_size: 32
    .language:       OpenCL C
    .language_version:
      - 2
      - 0
    .max_flat_workgroup_size: 256
    .name:           _Z6gbuildPKfS0_PfS1_
    .private_segment_fixed_size: 0
    .sgpr_count:     16
    .sgpr_spill_count: 0
    .symbol:         _Z6gbuildPKfS0_PfS1_.kd
    .uniform_work_group_size: 1
    .uses_dynamic_stack: false
    .vgpr_count:     28
    .vgpr_spill_count: 0
    .wavefront_size: 64
  - .agpr_count:     0
    .args:
      - .actual_access:  read_only
        .address_space:  global
        .offset:         0
        .size:           8
        .value_kind:     global_buffer
      - .actual_access:  read_only
        .address_space:  global
        .offset:         8
        .size:           8
        .value_kind:     global_buffer
      - .actual_access:  read_only
        .address_space:  global
        .offset:         16
        .size:           8
        .value_kind:     global_buffer
      - .actual_access:  read_only
        .address_space:  global
        .offset:         24
        .size:           8
        .value_kind:     global_buffer
      - .actual_access:  read_only
        .address_space:  global
        .offset:         32
        .size:           8
        .value_kind:     global_buffer
      - .actual_access:  read_only
        .address_space:  global
        .offset:         40
        .size:           8
        .value_kind:     global_buffer
      - .actual_access:  read_only
        .address_space:  global
        .offset:         48
        .size:           8
        .value_kind:     global_buffer
      - .actual_access:  read_only
        .address_space:  global
        .offset:         56
        .size:           8
        .value_kind:     global_buffer
      - .actual_access:  read_only
        .address_space:  global
        .offset:         64
        .size:           8
        .value_kind:     global_buffer
      - .actual_access:  write_only
        .address_space:  global
        .offset:         72
        .size:           8
        .value_kind:     global_buffer
    .group_segment_fixed_size: 0
    .kernarg_segment_align: 8
    .kernarg_segment_size: 80
    .language:       OpenCL C
    .language_version:
      - 2
      - 0
    .max_flat_workgroup_size: 256
    .name:           _Z13outproj_naivePKtS0_PKfS2_S2_S2_S2_S2_S2_Pf
    .private_segment_fixed_size: 0
    .sgpr_count:     37
    .sgpr_spill_count: 0
    .symbol:         _Z13outproj_naivePKtS0_PKfS2_S2_S2_S2_S2_S2_Pf.kd
    .uniform_work_group_size: 1
    .uses_dynamic_stack: false
    .vgpr_count:     20
    .vgpr_spill_count: 0
    .wavefront_size: 64
  - .agpr_count:     128
    .args:
      - .actual_access:  read_only
        .address_space:  global
        .offset:         0
        .size:           8
        .value_kind:     global_buffer
      - .actual_access:  read_only
        .address_space:  global
        .offset:         8
        .size:           8
        .value_kind:     global_buffer
      - .actual_access:  read_only
        .address_space:  global
        .offset:         16
        .size:           8
        .value_kind:     global_buffer
      - .actual_access:  read_only
        .address_space:  global
        .offset:         24
        .size:           8
        .value_kind:     global_buffer
      - .actual_access:  read_only
        .address_space:  global
        .offset:         32
        .size:           8
        .value_kind:     global_buffer
      - .actual_access:  read_only
        .address_space:  global
        .offset:         40
        .size:           8
        .value_kind:     global_buffer
      - .actual_access:  read_only
        .address_space:  global
        .offset:         48
        .size:           8
        .value_kind:     global_buffer
      - .actual_access:  read_only
        .address_space:  global
        .offset:         56
        .size:           8
        .value_kind:     global_buffer
      - .actual_access:  read_only
        .address_space:  global
        .offset:         64
        .size:           8
        .value_kind:     global_buffer
      - .actual_access:  write_only
        .address_space:  global
        .offset:         72
        .size:           8
        .value_kind:     global_buffer
    .group_segment_fixed_size: 0
    .kernarg_segment_align: 8
    .kernarg_segment_size: 80
    .language:       OpenCL C
    .language_version:
      - 2
      - 0
    .max_flat_workgroup_size: 256
    .name:           _Z12outproj_mfmaPKtS0_PKfS2_S2_S2_S2_S2_S2_Pf
    .private_segment_fixed_size: 0
    .sgpr_count:     30
    .sgpr_spill_count: 0
    .symbol:         _Z12outproj_mfmaPKtS0_PKfS2_S2_S2_S2_S2_S2_Pf.kd
    .uniform_work_group_size: 1
    .uses_dynamic_stack: false
    .vgpr_count:     384
    .vgpr_spill_count: 0
    .wavefront_size: 64
  - .agpr_count:     28
    .args:
      - .address_space:  global
        .offset:         0
        .size:           8
        .value_kind:     global_buffer
      - .actual_access:  read_only
        .address_space:  global
        .offset:         8
        .size:           8
        .value_kind:     global_buffer
      - .actual_access:  read_only
        .address_space:  global
        .offset:         16
        .size:           8
        .value_kind:     global_buffer
      - .actual_access:  read_only
        .address_space:  global
        .offset:         24
        .size:           8
        .value_kind:     global_buffer
      - .actual_access:  read_only
        .address_space:  global
        .offset:         32
        .size:           8
        .value_kind:     global_buffer
      - .actual_access:  read_only
        .address_space:  global
        .offset:         40
        .size:           8
        .value_kind:     global_buffer
    .group_segment_fixed_size: 5632
    .kernarg_segment_align: 8
    .kernarg_segment_size: 48
    .language:       OpenCL C
    .language_version:
      - 2
      - 0
    .max_flat_workgroup_size: 256
    .name:           _Z12gattn_kernelPfPKfS1_S1_S1_S1_
    .private_segment_fixed_size: 0
    .sgpr_count:     98
    .sgpr_spill_count: 0
    .symbol:         _Z12gattn_kernelPfPKfS1_S1_S1_S1_.kd
    .uniform_work_group_size: 1
    .uses_dynamic_stack: false
    .vgpr_count:     284
    .vgpr_spill_count: 0
    .wavefront_size: 64
  - .agpr_count:     0
    .args:
      - .actual_access:  read_only
        .address_space:  global
        .offset:         0
        .size:           8
        .value_kind:     global_buffer
      - .actual_access:  read_only
        .address_space:  global
        .offset:         8
        .size:           8
        .value_kind:     global_buffer
      - .actual_access:  read_only
        .address_space:  global
        .offset:         16
        .size:           8
        .value_kind:     global_buffer
      - .actual_access:  read_only
        .address_space:  global
        .offset:         24
        .size:           8
        .value_kind:     global_buffer
      - .actual_access:  read_only
        .address_space:  global
        .offset:         32
        .size:           8
        .value_kind:     global_buffer
      - .actual_access:  write_only
        .address_space:  global
        .offset:         40
        .size:           8
        .value_kind:     global_buffer
      - .actual_access:  write_only
        .address_space:  global
        .offset:         48
        .size:           8
        .value_kind:     global_buffer
      - .actual_access:  write_only
        .address_space:  global
        .offset:         56
        .size:           8
        .value_kind:     global_buffer
      - .actual_access:  read_only
        .address_space:  global
        .offset:         64
        .size:           8
        .value_kind:     global_buffer
      - .actual_access:  write_only
        .address_space:  global
        .offset:         72
        .size:           8
        .value_kind:     global_buffer
    .group_segment_fixed_size: 11264
    .kernarg_segment_align: 8
    .kernarg_segment_size: 80
    .language:       OpenCL C
    .language_version:
      - 2
      - 0
    .max_flat_workgroup_size: 1024
    .name:           _Z14special_kernelPKtPKfS2_S2_S2_PfS3_S3_S2_S3_
    .private_segment_fixed_size: 0
    .sgpr_count:     29
    .sgpr_spill_count: 0
    .symbol:         _Z14special_kernelPKtPKfS2_S2_S2_PfS3_S3_S2_S3_.kd
    .uniform_work_group_size: 1
    .uses_dynamic_stack: false
    .vgpr_count:     72
    .vgpr_spill_count: 0
    .wavefront_size: 64
  - .agpr_count:     0
    .args:
      - .actual_access:  read_only
        .address_space:  global
        .offset:         0
        .size:           8
        .value_kind:     global_buffer
      - .actual_access:  read_only
        .address_space:  global
        .offset:         8
        .size:           8
        .value_kind:     global_buffer
      - .actual_access:  read_only
        .address_space:  global
        .offset:         16
        .size:           8
        .value_kind:     global_buffer
      - .actual_access:  read_only
        .address_space:  global
        .offset:         24
        .size:           8
        .value_kind:     global_buffer
      - .actual_access:  read_only
        .address_space:  global
        .offset:         32
        .size:           8
        .value_kind:     global_buffer
      - .actual_access:  read_only
        .address_space:  global
        .offset:         40
        .size:           8
        .value_kind:     global_buffer
      - .actual_access:  read_only
        .address_space:  global
        .offset:         48
        .size:           8
        .value_kind:     global_buffer
      - .actual_access:  read_only
        .address_space:  global
        .offset:         56
        .size:           8
        .value_kind:     global_buffer
      - .actual_access:  read_only
        .address_space:  global
        .offset:         64
        .size:           8
        .value_kind:     global_buffer
      - .actual_access:  read_only
        .address_space:  global
        .offset:         72
        .size:           8
        .value_kind:     global_buffer
      - .actual_access:  read_only
        .address_space:  global
        .offset:         80
        .size:           8
        .value_kind:     global_buffer
      - .actual_access:  read_only
        .address_space:  global
        .offset:         88
        .size:           8
        .value_kind:     global_buffer
      - .actual_access:  read_only
        .address_space:  global
        .offset:         96
        .size:           8
        .value_kind:     global_buffer
      - .actual_access:  read_only
        .address_space:  global
        .offset:         104
        .size:           8
        .value_kind:     global_buffer
      - .actual_access:  write_only
        .address_space:  global
        .offset:         112
        .size:           8
        .value_kind:     global_buffer
      - .actual_access:  read_only
        .address_space:  global
        .offset:         120
        .size:           8
        .value_kind:     global_buffer
      - .address_space:  global
        .offset:         128
        .size:           8
        .value_kind:     global_buffer
    .group_segment_fixed_size: 74240
    .kernarg_segment_align: 8
    .kernarg_segment_size: 136
    .language:       OpenCL C
    .language_version:
      - 2
      - 0
    .max_flat_workgroup_size: 512
    .name:           _Z12final_kernelPKtS0_PKfS2_S2_S2_S2_S2_S2_S2_S2_S2_S2_S2_PfPKhS5_
    .private_segment_fixed_size: 0
    .sgpr_count:     34
    .sgpr_spill_count: 0
    .symbol:         _Z12final_kernelPKtS0_PKfS2_S2_S2_S2_S2_S2_S2_S2_S2_S2_S2_PfPKhS5_.kd
    .uniform_work_group_size: 1
    .uses_dynamic_stack: false
    .vgpr_count:     128
    .vgpr_spill_count: 0
    .wavefront_size: 64
